# v45 + per-workgroup chunk size 7/8/9 by row count (bandwidth share proportional to work)
# baseline (speedup 1.0000x reference)
.Lfront_nocursor:
	s_waitcnt lgkmcnt(0)
	s_barrier
	s_mov_b64 exec, s[36:37]
	ds_add_rtn_u32 v106, v74, v143 offset:34820
	s_mov_b64 exec, s[38:39]
	ds_add_rtn_u32 v107, v75, v143 offset:34820
	s_mov_b64 exec, s[40:41]
	ds_add_rtn_u32 v108, v76, v143 offset:34820
	s_mov_b64 exec, s[42:43]
	ds_add_rtn_u32 v109, v77, v143 offset:34820
	s_mov_b64 exec, s[44:45]
	ds_add_rtn_u32 v110, v78, v143 offset:34820
	s_mov_b64 exec, s[46:47]
	ds_add_rtn_u32 v111, v79, v143 offset:34820
	s_mov_b64 exec, s[48:49]
	ds_add_rtn_u32 v112, v80, v143 offset:34820
	s_mov_b64 exec, s[50:51]
	ds_add_rtn_u32 v113, v81, v143 offset:34820
	s_mov_b64 exec, s[52:53]
	ds_add_rtn_u32 v114, v82, v143 offset:34820
	s_mov_b64 exec, s[54:55]
	ds_add_rtn_u32 v115, v83, v143 offset:34820
	s_mov_b64 exec, s[56:57]
	ds_add_rtn_u32 v116, v84, v143 offset:34820
	s_mov_b64 exec, s[58:59]
	ds_add_rtn_u32 v117, v85, v143 offset:34820
	s_mov_b64 exec, s[60:61]
	ds_add_rtn_u32 v118, v86, v143 offset:34820
	s_mov_b64 exec, s[62:63]
	ds_add_rtn_u32 v119, v87, v143 offset:34820
	s_mov_b64 exec, s[64:65]
	ds_add_rtn_u32 v120, v88, v143 offset:34820
	s_mov_b64 exec, s[66:67]
	ds_add_rtn_u32 v121, v89, v143 offset:34820
	s_mov_b64 exec, s[68:69]
	ds_add_rtn_u32 v122, v90, v143 offset:34820
	s_mov_b64 exec, s[70:71]
	ds_add_rtn_u32 v123, v91, v143 offset:34820
	s_mov_b64 exec, s[72:73]
	ds_add_rtn_u32 v124, v92, v143 offset:34820
	s_mov_b64 exec, s[74:75]
	ds_add_rtn_u32 v125, v93, v143 offset:34820
	s_mov_b64 exec, s[76:77]
	ds_add_rtn_u32 v126, v94, v143 offset:34820
	s_mov_b64 exec, s[78:79]
	ds_add_rtn_u32 v127, v95, v143 offset:34820
	s_mov_b64 exec, s[80:81]
	ds_add_rtn_u32 v128, v96, v143 offset:34820
	s_mov_b64 exec, s[82:83]
	ds_add_rtn_u32 v129, v97, v143 offset:34820
	s_mov_b64 exec, s[84:85]
	ds_add_rtn_u32 v130, v98, v143 offset:34820
	s_mov_b64 exec, s[86:87]
	ds_add_rtn_u32 v131, v99, v143 offset:34820
	s_mov_b64 exec, s[88:89]
	ds_add_rtn_u32 v132, v100, v143 offset:34820
	s_mov_b64 exec, s[90:91]
	ds_add_rtn_u32 v133, v101, v143 offset:34820
	s_mov_b64 exec, s[92:93]
	ds_add_rtn_u32 v134, v102, v143 offset:34820
	s_mov_b64 exec, s[94:95]
	ds_add_rtn_u32 v135, v103, v143 offset:34820
	s_mov_b64 exec, s[96:97]
	ds_add_rtn_u32 v136, v104, v143 offset:34820
	s_mov_b64 exec, s[98:99]
	ds_add_rtn_u32 v137, v105, v143 offset:34820
	s_mov_b64 exec, -1
	v_lshlrev_b32_e32 v145, 18, v0
	v_add_u32_e32 v146, 0x0, v145
	v_or_b32_e32 v74, v146, v74
	v_add_u32_e32 v147, 0x10000, v145
	v_or_b32_e32 v75, v147, v75
	v_add_u32_e32 v146, 0x20000, v145
	v_or_b32_e32 v76, v146, v76
	v_add_u32_e32 v147, 0x30000, v145
	v_or_b32_e32 v77, v147, v77
	v_add_u32_e32 v146, 0x4000000, v145
	v_or_b32_e32 v78, v146, v78
	v_add_u32_e32 v147, 0x4010000, v145
	v_or_b32_e32 v79, v147, v79
	v_add_u32_e32 v146, 0x4020000, v145
	v_or_b32_e32 v80, v146, v80
	v_add_u32_e32 v147, 0x4030000, v145
	v_or_b32_e32 v81, v147, v81
	v_add_u32_e32 v146, 0x8000000, v145
	v_or_b32_e32 v82, v146, v82
	v_add_u32_e32 v147, 0x8010000, v145
	v_or_b32_e32 v83, v147, v83
	v_add_u32_e32 v146, 0x8020000, v145
	v_or_b32_e32 v84, v146, v84
	v_add_u32_e32 v147, 0x8030000, v145
	v_or_b32_e32 v85, v147, v85
	v_add_u32_e32 v146, 0xc000000, v145
	v_or_b32_e32 v86, v146, v86
	v_add_u32_e32 v147, 0xc010000, v145
	v_or_b32_e32 v87, v147, v87
	v_add_u32_e32 v146, 0xc020000, v145
	v_or_b32_e32 v88, v146, v88
	v_add_u32_e32 v147, 0xc030000, v145
	v_or_b32_e32 v89, v147, v89
	v_add_u32_e32 v146, 0x10000000, v145
	v_or_b32_e32 v90, v146, v90
	v_add_u32_e32 v147, 0x10010000, v145
	v_or_b32_e32 v91, v147, v91
	v_add_u32_e32 v146, 0x10020000, v145
	v_or_b32_e32 v92, v146, v92
	v_add_u32_e32 v147, 0x10030000, v145
	v_or_b32_e32 v93, v147, v93
	v_add_u32_e32 v146, 0x14000000, v145
	v_or_b32_e32 v94, v146, v94
	v_add_u32_e32 v147, 0x14010000, v145
	v_or_b32_e32 v95, v147, v95
	v_add_u32_e32 v146, 0x14020000, v145
	v_or_b32_e32 v96, v146, v96
	v_add_u32_e32 v147, 0x14030000, v145
	v_or_b32_e32 v97, v147, v97
	v_add_u32_e32 v146, 0x18000000, v145
	v_or_b32_e32 v98, v146, v98
	v_add_u32_e32 v147, 0x18010000, v145
	v_or_b32_e32 v99, v147, v99
	v_add_u32_e32 v146, 0x18020000, v145
	v_or_b32_e32 v100, v146, v100
	v_add_u32_e32 v147, 0x18030000, v145
	v_or_b32_e32 v101, v147, v101
	v_add_u32_e32 v146, 0x1c000000, v145
	v_or_b32_e32 v102, v146, v102
	v_add_u32_e32 v147, 0x1c010000, v145
	v_or_b32_e32 v103, v147, v103
	v_add_u32_e32 v146, 0x1c020000, v145
	v_or_b32_e32 v104, v146, v104
	v_add_u32_e32 v147, 0x1c030000, v145
	v_or_b32_e32 v105, v147, v105
	s_waitcnt lgkmcnt(0)
	s_mov_b64 exec, s[36:37]
	ds_write_b32 v106, v74
	s_mov_b64 exec, s[38:39]
	ds_write_b32 v107, v75
	s_mov_b64 exec, s[40:41]
	ds_write_b32 v108, v76
	s_mov_b64 exec, s[42:43]
	ds_write_b32 v109, v77
	s_mov_b64 exec, s[44:45]
	ds_write_b32 v110, v78
	s_mov_b64 exec, s[46:47]
	ds_write_b32 v111, v79
	s_mov_b64 exec, s[48:49]
	ds_write_b32 v112, v80
	s_mov_b64 exec, s[50:51]
	ds_write_b32 v113, v81
	s_mov_b64 exec, s[52:53]
	ds_write_b32 v114, v82
	s_mov_b64 exec, s[54:55]
	ds_write_b32 v115, v83
	s_mov_b64 exec, s[56:57]
	ds_write_b32 v116, v84
	s_mov_b64 exec, s[58:59]
	ds_write_b32 v117, v85
	s_mov_b64 exec, s[60:61]
	ds_write_b32 v118, v86
	s_mov_b64 exec, s[62:63]
	ds_write_b32 v119, v87
	s_mov_b64 exec, s[64:65]
	ds_write_b32 v120, v88
	s_mov_b64 exec, s[66:67]
	ds_write_b32 v121, v89
	s_mov_b64 exec, s[68:69]
	ds_write_b32 v122, v90
	s_mov_b64 exec, s[70:71]
	ds_write_b32 v123, v91
	s_mov_b64 exec, s[72:73]
	ds_write_b32 v124, v92
	s_mov_b64 exec, s[74:75]
	ds_write_b32 v125, v93
	s_mov_b64 exec, s[76:77]
	ds_write_b32 v126, v94
	s_mov_b64 exec, s[78:79]
	ds_write_b32 v127, v95
	s_mov_b64 exec, s[80:81]
	ds_write_b32 v128, v96
	s_mov_b64 exec, s[82:83]
	ds_write_b32 v129, v97
	s_mov_b64 exec, s[84:85]
	ds_write_b32 v130, v98
	s_mov_b64 exec, s[86:87]
	ds_write_b32 v131, v99
	s_mov_b64 exec, s[88:89]
	ds_write_b32 v132, v100
	s_mov_b64 exec, s[90:91]
	ds_write_b32 v133, v101
	s_mov_b64 exec, s[92:93]
	ds_write_b32 v134, v102
	s_mov_b64 exec, s[94:95]
	ds_write_b32 v135, v103
	s_mov_b64 exec, s[96:97]
	ds_write_b32 v136, v104
	s_mov_b64 exec, s[98:99]
	ds_write_b32 v137, v105
	s_mov_b64 exec, -1
	s_waitcnt lgkmcnt(0)
	s_barrier
	v_lshlrev_b32_e32 v218, 4, v1
	v_lshlrev_b32_e32 v219, 3, v1
	v_mov_b32_e32 v223, 0x11540
	v_bfrev_b32_e32 v199, 1
	v_mov_b32_e32 v198, 1
	v_and_b32_e32 v221, 15, v1
	v_mov_b32_e32 v200, 0
	v_mov_b32_e32 v201, 0
	v_mov_b32_e32 v202, 0
	v_mov_b32_e32 v203, 0
	v_mov_b32_e32 v204, 0
	v_mov_b32_e32 v205, 0
	v_mov_b32_e32 v206, 0
	v_mov_b32_e32 v207, 0
	s_mov_b32 s50, -1
	s_cmp_lt_u32 s8, 240
	s_cbranch_scc1 .Lg0_start
	s_cmp_lt_u32 s8, 272
	s_cbranch_scc1 .Lg1_start
	s_branch .Lg2_start
.Lg0_start:
	s_add_i32 s53, s8, 6
	s_mul_hi_u32 s53, s53, 0x92492493
	s_lshr_b32 s53, s53, 2
	s_mov_b32 s54, s17
	s_add_i32 s55, s17, 4
	s_cmp_ge_u32 s54, s53
	s_cbranch_scc1 .Lg_alldone
	s_mul_i32 s46, s54, 7
	v_add_u32_e32 v220, s46, v221
	v_cmp_gt_u32_e32 vcc, s8, v220
	v_lshlrev_b32_e32 v220, 2, v220
	ds_read_b32 v216, v220
	s_waitcnt lgkmcnt(0)
	v_cndmask_b32_e32 v216, v199, v216, vcc
	s_nop 1
	v_readlane_b32 s50, v216, 0
	s_and_b32 s50, s50, 0xffff
	v_readlane_b32 s40, v216, 0
	s_and_b32 s60, s40, 0xffff
	s_bitcmp1_b32 s40, 31
	s_cselect_b32 s60, 0xffff, s60
	s_bfe_u32 s40, s40, 0xd0010
	s_lshl_b32 s40, s40, 10
	s_add_u32 s42, s32, s40
	s_addc_u32 s43, s33, 0
	global_load_dwordx4 v[66:69], v218, s[42:43] nt
	v_readlane_b32 s40, v216, 1
	s_and_b32 s61, s40, 0xffff
	s_bitcmp1_b32 s40, 31
	s_cselect_b32 s61, 0xffff, s61
	s_bfe_u32 s40, s40, 0xd0010
	s_lshl_b32 s40, s40, 10
	s_add_u32 s42, s32, s40
	s_addc_u32 s43, s33, 0
	global_load_dwordx4 v[70:73], v218, s[42:43] nt
	v_readlane_b32 s40, v216, 2
	s_and_b32 s62, s40, 0xffff
	s_bitcmp1_b32 s40, 31
	s_cselect_b32 s62, 0xffff, s62
	s_bfe_u32 s40, s40, 0xd0010
	s_lshl_b32 s40, s40, 10
	s_add_u32 s42, s32, s40
	s_addc_u32 s43, s33, 0
	global_load_dwordx4 v[74:77], v218, s[42:43] nt
	v_readlane_b32 s40, v216, 3
	s_and_b32 s63, s40, 0xffff
	s_bitcmp1_b32 s40, 31
	s_cselect_b32 s63, 0xffff, s63
	s_bfe_u32 s40, s40, 0xd0010
	s_lshl_b32 s40, s40, 10
	s_add_u32 s42, s32, s40
	s_addc_u32 s43, s33, 0
	global_load_dwordx4 v[78:81], v218, s[42:43] nt
	v_readlane_b32 s40, v216, 4
	s_and_b32 s64, s40, 0xffff
	s_bitcmp1_b32 s40, 31
	s_cselect_b32 s64, 0xffff, s64
	s_bfe_u32 s40, s40, 0xd0010
	s_lshl_b32 s40, s40, 10
	s_add_u32 s42, s32, s40
	s_addc_u32 s43, s33, 0
	global_load_dwordx4 v[82:85], v218, s[42:43] nt
	v_readlane_b32 s40, v216, 5
	s_and_b32 s65, s40, 0xffff
	s_bitcmp1_b32 s40, 31
	s_cselect_b32 s65, 0xffff, s65
	s_bfe_u32 s40, s40, 0xd0010
	s_lshl_b32 s40, s40, 10
	s_add_u32 s42, s32, s40
	s_addc_u32 s43, s33, 0
	global_load_dwordx4 v[86:89], v218, s[42:43] nt
	v_readlane_b32 s40, v216, 6
	s_and_b32 s66, s40, 0xffff
	s_bitcmp1_b32 s40, 31
	s_cselect_b32 s66, 0xffff, s66
	s_bfe_u32 s40, s40, 0xd0010
	s_lshl_b32 s40, s40, 10
	s_add_u32 s42, s32, s40
	s_addc_u32 s43, s33, 0
	global_load_dwordx4 v[90:93], v218, s[42:43] nt
	s_cmp_ge_u32 s55, s53
	s_cbranch_scc1 .Lg0_drainA
	s_mul_i32 s46, s55, 7
	v_add_u32_e32 v220, s46, v221
	v_cmp_gt_u32_e32 vcc, s8, v220
	v_lshlrev_b32_e32 v220, 2, v220
	ds_read_b32 v217, v220
	s_waitcnt lgkmcnt(0)
	v_cndmask_b32_e32 v217, v199, v217, vcc
	s_nop 1
	v_readlane_b32 s40, v217, 0
	s_and_b32 s67, s40, 0xffff
	s_bitcmp1_b32 s40, 31
	s_cselect_b32 s67, 0xffff, s67
	s_bfe_u32 s40, s40, 0xd0010
	s_lshl_b32 s40, s40, 10
	s_add_u32 s42, s32, s40
	s_addc_u32 s43, s33, 0
	global_load_dwordx4 v[94:97], v218, s[42:43] nt
	v_readlane_b32 s40, v217, 1
	s_and_b32 s68, s40, 0xffff
	s_bitcmp1_b32 s40, 31
	s_cselect_b32 s68, 0xffff, s68
	s_bfe_u32 s40, s40, 0xd0010
	s_lshl_b32 s40, s40, 10
	s_add_u32 s42, s32, s40
	s_addc_u32 s43, s33, 0
	global_load_dwordx4 v[98:101], v218, s[42:43] nt
	v_readlane_b32 s40, v217, 2
	s_and_b32 s69, s40, 0xffff
	s_bitcmp1_b32 s40, 31
	s_cselect_b32 s69, 0xffff, s69
	s_bfe_u32 s40, s40, 0xd0010
	s_lshl_b32 s40, s40, 10
	s_add_u32 s42, s32, s40
	s_addc_u32 s43, s33, 0
	global_load_dwordx4 v[102:105], v218, s[42:43] nt
	v_readlane_b32 s40, v217, 3
	s_and_b32 s70, s40, 0xffff
	s_bitcmp1_b32 s40, 31
	s_cselect_b32 s70, 0xffff, s70
	s_bfe_u32 s40, s40, 0xd0010
	s_lshl_b32 s40, s40, 10
	s_add_u32 s42, s32, s40
	s_addc_u32 s43, s33, 0
	global_load_dwordx4 v[106:109], v218, s[42:43] nt
	v_readlane_b32 s40, v217, 4
	s_and_b32 s71, s40, 0xffff
	s_bitcmp1_b32 s40, 31
	s_cselect_b32 s71, 0xffff, s71
	s_bfe_u32 s40, s40, 0xd0010
	s_lshl_b32 s40, s40, 10
	s_add_u32 s42, s32, s40
	s_addc_u32 s43, s33, 0
	global_load_dwordx4 v[110:113], v218, s[42:43] nt
	v_readlane_b32 s40, v217, 5
	s_and_b32 s72, s40, 0xffff
	s_bitcmp1_b32 s40, 31
	s_cselect_b32 s72, 0xffff, s72
	s_bfe_u32 s40, s40, 0xd0010
	s_lshl_b32 s40, s40, 10
	s_add_u32 s42, s32, s40
	s_addc_u32 s43, s33, 0
	global_load_dwordx4 v[114:117], v218, s[42:43] nt
	v_readlane_b32 s40, v217, 6
	s_and_b32 s73, s40, 0xffff
	s_bitcmp1_b32 s40, 31
	s_cselect_b32 s73, 0xffff, s73
	s_bfe_u32 s40, s40, 0xd0010
	s_lshl_b32 s40, s40, 10
	s_add_u32 s42, s32, s40
	s_addc_u32 s43, s33, 0
	global_load_dwordx4 v[118:121], v218, s[42:43] nt
.Lg0_loop:
	s_mov_b64 exec, 1
	ds_add_rtn_u32 v222, v223, v198
	s_mov_b64 exec, -1
	s_waitcnt vmcnt(13)
	s_cmp_eq_u32 s60, 0xffff
	s_cbranch_scc1 .Lg0_A8_skip0
	s_cmp_lg_u32 s60, s50
	s_cbranch_scc1 .Lg0_A8_flush0

.Lg0_A8_skip0:
	s_waitcnt vmcnt(12)
	s_cmp_eq_u32 s61, 0xffff
	s_cbranch_scc1 .Lg0_A8_skip1
	s_cmp_lg_u32 s61, s50
	s_cbranch_scc1 .Lg0_A8_flush1

.Lg0_A8_skip1:
	s_waitcnt vmcnt(11)
	s_cmp_eq_u32 s62, 0xffff
	s_cbranch_scc1 .Lg0_A8_skip2
	s_cmp_lg_u32 s62, s50
	s_cbranch_scc1 .Lg0_A8_flush2

.Lg0_A8_skip2:
	s_waitcnt vmcnt(10)
	s_cmp_eq_u32 s63, 0xffff
	s_cbranch_scc1 .Lg0_A8_skip3
	s_cmp_lg_u32 s63, s50
	s_cbranch_scc1 .Lg0_A8_flush3

.Lg0_A8_skip3:
	s_waitcnt vmcnt(9)
	s_cmp_eq_u32 s64, 0xffff
	s_cbranch_scc1 .Lg0_A8_skip4
	s_cmp_lg_u32 s64, s50
	s_cbranch_scc1 .Lg0_A8_flush4

.Lg0_A8_skip4:
	s_waitcnt vmcnt(8)
	s_cmp_eq_u32 s65, 0xffff
	s_cbranch_scc1 .Lg0_A8_skip5
	s_cmp_lg_u32 s65, s50
	s_cbranch_scc1 .Lg0_A8_flush5

.Lg0_A8_skip5:
	s_waitcnt vmcnt(7)
	s_cmp_eq_u32 s66, 0xffff
	s_cbranch_scc1 .Lg0_A8_skip6
	s_cmp_lg_u32 s66, s50
	s_cbranch_scc1 .Lg0_A8_flush6

.Lg0_A8_skip6:
	s_waitcnt lgkmcnt(0)
	v_readfirstlane_b32 s54, v222
	s_cmp_ge_u32 s54, s53
	s_cbranch_scc1 .Lg0_drainB
	s_mul_i32 s46, s54, 7
	v_add_u32_e32 v220, s46, v221
	v_cmp_gt_u32_e32 vcc, s8, v220
	v_lshlrev_b32_e32 v220, 2, v220
	ds_read_b32 v216, v220
	s_waitcnt lgkmcnt(0)
	v_cndmask_b32_e32 v216, v199, v216, vcc
	s_nop 1
	v_readlane_b32 s40, v216, 0
	s_and_b32 s60, s40, 0xffff
	s_bitcmp1_b32 s40, 31
	s_cselect_b32 s60, 0xffff, s60
	s_bfe_u32 s40, s40, 0xd0010
	s_lshl_b32 s40, s40, 10
	s_add_u32 s42, s32, s40
	s_addc_u32 s43, s33, 0
	global_load_dwordx4 v[66:69], v218, s[42:43] nt
	v_readlane_b32 s40, v216, 1
	s_and_b32 s61, s40, 0xffff
	s_bitcmp1_b32 s40, 31
	s_cselect_b32 s61, 0xffff, s61
	s_bfe_u32 s40, s40, 0xd0010
	s_lshl_b32 s40, s40, 10
	s_add_u32 s42, s32, s40
	s_addc_u32 s43, s33, 0
	global_load_dwordx4 v[70:73], v218, s[42:43] nt
	v_readlane_b32 s40, v216, 2
	s_and_b32 s62, s40, 0xffff
	s_bitcmp1_b32 s40, 31
	s_cselect_b32 s62, 0xffff, s62
	s_bfe_u32 s40, s40, 0xd0010
	s_lshl_b32 s40, s40, 10
	s_add_u32 s42, s32, s40
	s_addc_u32 s43, s33, 0
	global_load_dwordx4 v[74:77], v218, s[42:43] nt
	v_readlane_b32 s40, v216, 3
	s_and_b32 s63, s40, 0xffff
	s_bitcmp1_b32 s40, 31
	s_cselect_b32 s63, 0xffff, s63
	s_bfe_u32 s40, s40, 0xd0010
	s_lshl_b32 s40, s40, 10
	s_add_u32 s42, s32, s40
	s_addc_u32 s43, s33, 0
	global_load_dwordx4 v[78:81], v218, s[42:43] nt
	v_readlane_b32 s40, v216, 4
	s_and_b32 s64, s40, 0xffff
	s_bitcmp1_b32 s40, 31
	s_cselect_b32 s64, 0xffff, s64
	s_bfe_u32 s40, s40, 0xd0010
	s_lshl_b32 s40, s40, 10
	s_add_u32 s42, s32, s40
	s_addc_u32 s43, s33, 0
	global_load_dwordx4 v[82:85], v218, s[42:43] nt
	v_readlane_b32 s40, v216, 5
	s_and_b32 s65, s40, 0xffff
	s_bitcmp1_b32 s40, 31
	s_cselect_b32 s65, 0xffff, s65
	s_bfe_u32 s40, s40, 0xd0010
	s_lshl_b32 s40, s40, 10
	s_add_u32 s42, s32, s40
	s_addc_u32 s43, s33, 0
	global_load_dwordx4 v[86:89], v218, s[42:43] nt
	v_readlane_b32 s40, v216, 6
	s_and_b32 s66, s40, 0xffff
	s_bitcmp1_b32 s40, 31
	s_cselect_b32 s66, 0xffff, s66
	s_bfe_u32 s40, s40, 0xd0010
	s_lshl_b32 s40, s40, 10
	s_add_u32 s42, s32, s40
	s_addc_u32 s43, s33, 0
	global_load_dwordx4 v[90:93], v218, s[42:43] nt
	s_mov_b64 exec, 1
	ds_add_rtn_u32 v222, v223, v198
	s_mov_b64 exec, -1
	s_waitcnt vmcnt(13)
	s_cmp_eq_u32 s67, 0xffff
	s_cbranch_scc1 .Lg0_B8_skip7
	s_cmp_lg_u32 s67, s50
	s_cbranch_scc1 .Lg0_B8_flush7

.Lg0_B8_skip7:
	s_waitcnt vmcnt(12)
	s_cmp_eq_u32 s68, 0xffff
	s_cbranch_scc1 .Lg0_B8_skip8
	s_cmp_lg_u32 s68, s50
	s_cbranch_scc1 .Lg0_B8_flush8

.Lg0_B8_skip8:
	s_waitcnt vmcnt(11)
	s_cmp_eq_u32 s69, 0xffff
	s_cbranch_scc1 .Lg0_B8_skip9
	s_cmp_lg_u32 s69, s50
	s_cbranch_scc1 .Lg0_B8_flush9

.Lg0_B8_skip9:
	s_waitcnt vmcnt(10)
	s_cmp_eq_u32 s70, 0xffff
	s_cbranch_scc1 .Lg0_B8_skip10
	s_cmp_lg_u32 s70, s50
	s_cbranch_scc1 .Lg0_B8_flush10

.Lg0_B8_skip10:
	s_waitcnt vmcnt(9)
	s_cmp_eq_u32 s71, 0xffff
	s_cbranch_scc1 .Lg0_B8_skip11
	s_cmp_lg_u32 s71, s50
	s_cbranch_scc1 .Lg0_B8_flush11

.Lg0_B8_skip11:
	s_waitcnt vmcnt(8)
	s_cmp_eq_u32 s72, 0xffff
	s_cbranch_scc1 .Lg0_B8_skip12
	s_cmp_lg_u32 s72, s50
	s_cbranch_scc1 .Lg0_B8_flush12

.Lg0_B8_skip12:
	s_waitcnt vmcnt(7)
	s_cmp_eq_u32 s73, 0xffff
	s_cbranch_scc1 .Lg0_B8_skip13
	s_cmp_lg_u32 s73, s50
	s_cbranch_scc1 .Lg0_B8_flush13

.Lg0_B8_skip13:
	s_waitcnt lgkmcnt(0)
	v_readfirstlane_b32 s55, v222
	s_cmp_ge_u32 s55, s53
	s_cbranch_scc1 .Lg0_drainA
	s_mul_i32 s46, s55, 7
	v_add_u32_e32 v220, s46, v221
	v_cmp_gt_u32_e32 vcc, s8, v220
	v_lshlrev_b32_e32 v220, 2, v220
	ds_read_b32 v217, v220
	s_waitcnt lgkmcnt(0)
	v_cndmask_b32_e32 v217, v199, v217, vcc
	s_nop 1
	v_readlane_b32 s40, v217, 0
	s_and_b32 s67, s40, 0xffff
	s_bitcmp1_b32 s40, 31
	s_cselect_b32 s67, 0xffff, s67
	s_bfe_u32 s40, s40, 0xd0010
	s_lshl_b32 s40, s40, 10
	s_add_u32 s42, s32, s40
	s_addc_u32 s43, s33, 0
	global_load_dwordx4 v[94:97], v218, s[42:43] nt
	v_readlane_b32 s40, v217, 1
	s_and_b32 s68, s40, 0xffff
	s_bitcmp1_b32 s40, 31
	s_cselect_b32 s68, 0xffff, s68
	s_bfe_u32 s40, s40, 0xd0010
	s_lshl_b32 s40, s40, 10
	s_add_u32 s42, s32, s40
	s_addc_u32 s43, s33, 0
	global_load_dwordx4 v[98:101], v218, s[42:43] nt
	v_readlane_b32 s40, v217, 2
	s_and_b32 s69, s40, 0xffff
	s_bitcmp1_b32 s40, 31
	s_cselect_b32 s69, 0xffff, s69
	s_bfe_u32 s40, s40, 0xd0010
	s_lshl_b32 s40, s40, 10
	s_add_u32 s42, s32, s40
	s_addc_u32 s43, s33, 0
	global_load_dwordx4 v[102:105], v218, s[42:43] nt
	v_readlane_b32 s40, v217, 3
	s_and_b32 s70, s40, 0xffff
	s_bitcmp1_b32 s40, 31
	s_cselect_b32 s70, 0xffff, s70
	s_bfe_u32 s40, s40, 0xd0010
	s_lshl_b32 s40, s40, 10
	s_add_u32 s42, s32, s40
	s_addc_u32 s43, s33, 0
	global_load_dwordx4 v[106:109], v218, s[42:43] nt
	v_readlane_b32 s40, v217, 4
	s_and_b32 s71, s40, 0xffff
	s_bitcmp1_b32 s40, 31
	s_cselect_b32 s71, 0xffff, s71
	s_bfe_u32 s40, s40, 0xd0010
	s_lshl_b32 s40, s40, 10
	s_add_u32 s42, s32, s40
	s_addc_u32 s43, s33, 0
	global_load_dwordx4 v[110:113], v218, s[42:43] nt
	v_readlane_b32 s40, v217, 5
	s_and_b32 s72, s40, 0xffff
	s_bitcmp1_b32 s40, 31
	s_cselect_b32 s72, 0xffff, s72
	s_bfe_u32 s40, s40, 0xd0010
	s_lshl_b32 s40, s40, 10
	s_add_u32 s42, s32, s40
	s_addc_u32 s43, s33, 0
	global_load_dwordx4 v[114:117], v218, s[42:43] nt
	v_readlane_b32 s40, v217, 6
	s_and_b32 s73, s40, 0xffff
	s_bitcmp1_b32 s40, 31
	s_cselect_b32 s73, 0xffff, s73
	s_bfe_u32 s40, s40, 0xd0010
	s_lshl_b32 s40, s40, 10
	s_add_u32 s42, s32, s40
	s_addc_u32 s43, s33, 0
	global_load_dwordx4 v[118:121], v218, s[42:43] nt
	s_branch .Lg0_loop
.Lg0_drainA:
	s_waitcnt vmcnt(6)
	s_cmp_eq_u32 s60, 0xffff
	s_cbranch_scc1 .Lg0_A0_skip0
	s_cmp_lg_u32 s60, s50
	s_cbranch_scc1 .Lg0_A0_flush0

.Lg0_A0_skip0:
	s_waitcnt vmcnt(5)
	s_cmp_eq_u32 s61, 0xffff
	s_cbranch_scc1 .Lg0_A0_skip1
	s_cmp_lg_u32 s61, s50
	s_cbranch_scc1 .Lg0_A0_flush1

.Lg0_A0_skip1:
	s_waitcnt vmcnt(4)
	s_cmp_eq_u32 s62, 0xffff
	s_cbranch_scc1 .Lg0_A0_skip2
	s_cmp_lg_u32 s62, s50
	s_cbranch_scc1 .Lg0_A0_flush2

.Lg0_A0_skip2:
	s_waitcnt vmcnt(3)
	s_cmp_eq_u32 s63, 0xffff
	s_cbranch_scc1 .Lg0_A0_skip3
	s_cmp_lg_u32 s63, s50
	s_cbranch_scc1 .Lg0_A0_flush3

.Lg0_A0_skip3:
	s_waitcnt vmcnt(2)
	s_cmp_eq_u32 s64, 0xffff
	s_cbranch_scc1 .Lg0_A0_skip4
	s_cmp_lg_u32 s64, s50
	s_cbranch_scc1 .Lg0_A0_flush4

.Lg0_A0_skip4:
	s_waitcnt vmcnt(1)
	s_cmp_eq_u32 s65, 0xffff
	s_cbranch_scc1 .Lg0_A0_skip5
	s_cmp_lg_u32 s65, s50
	s_cbranch_scc1 .Lg0_A0_flush5

.Lg0_A0_skip5:
	s_waitcnt vmcnt(0)
	s_cmp_eq_u32 s66, 0xffff
	s_cbranch_scc1 .Lg0_A0_skip6
	s_cmp_lg_u32 s66, s50
	s_cbranch_scc1 .Lg0_A0_flush6
.Lg0_A0_cont6:
	v_cvt_f64_f32_e32 v[208:209], v90
	v_cvt_f64_f32_e32 v[210:211], v91
	v_cvt_f64_f32_e32 v[212:213], v92
	v_cvt_f64_f32_e32 v[214:215], v93
	v_add_f64 v[200:201], v[200:201], v[208:209]
	v_add_f64 v[202:203], v[202:203], v[210:211]
	v_add_f64 v[204:205], v[204:205], v[212:213]
	v_add_f64 v[206:207], v[206:207], v[214:215]
.Lg0_A0_skip6:
	s_branch .Lg0_fin
.Lg0_drainB:
	s_waitcnt vmcnt(6)
	s_cmp_eq_u32 s67, 0xffff
	s_cbranch_scc1 .Lg0_B0_skip7
	s_cmp_lg_u32 s67, s50
	s_cbranch_scc1 .Lg0_B0_flush7

.Lg0_B0_skip7:
	s_waitcnt vmcnt(5)
	s_cmp_eq_u32 s68, 0xffff
	s_cbranch_scc1 .Lg0_B0_skip8
	s_cmp_lg_u32 s68, s50
	s_cbranch_scc1 .Lg0_B0_flush8

.Lg0_B0_skip8:
	s_waitcnt vmcnt(4)
	s_cmp_eq_u32 s69, 0xffff
	s_cbranch_scc1 .Lg0_B0_skip9
	s_cmp_lg_u32 s69, s50
	s_cbranch_scc1 .Lg0_B0_flush9

.Lg0_B0_skip9:
	s_waitcnt vmcnt(3)
	s_cmp_eq_u32 s70, 0xffff
	s_cbranch_scc1 .Lg0_B0_skip10
	s_cmp_lg_u32 s70, s50
	s_cbranch_scc1 .Lg0_B0_flush10

.Lg0_B0_skip10:
	s_waitcnt vmcnt(2)
	s_cmp_eq_u32 s71, 0xffff
	s_cbranch_scc1 .Lg0_B0_skip11
	s_cmp_lg_u32 s71, s50
	s_cbranch_scc1 .Lg0_B0_flush11

.Lg0_B0_skip11:
	s_waitcnt vmcnt(1)
	s_cmp_eq_u32 s72, 0xffff
	s_cbranch_scc1 .Lg0_B0_skip12
	s_cmp_lg_u32 s72, s50
	s_cbranch_scc1 .Lg0_B0_flush12

.Lg0_B0_skip12:
	s_waitcnt vmcnt(0)
	s_cmp_eq_u32 s73, 0xffff
	s_cbranch_scc1 .Lg0_B0_skip13
	s_cmp_lg_u32 s73, s50
	s_cbranch_scc1 .Lg0_B0_flush13
.Lg0_B0_cont13:
	v_cvt_f64_f32_e32 v[208:209], v118
	v_cvt_f64_f32_e32 v[210:211], v119
	v_cvt_f64_f32_e32 v[212:213], v120
	v_cvt_f64_f32_e32 v[214:215], v121
	v_add_f64 v[200:201], v[200:201], v[208:209]
	v_add_f64 v[202:203], v[202:203], v[210:211]
	v_add_f64 v[204:205], v[204:205], v[212:213]
	v_add_f64 v[206:207], v[206:207], v[214:215]
.Lg0_B0_skip13:
.Lg0_fin:
	v_add_u32_e32 v220, s50, v219
	ds_add_f64 v220, v[200:201] offset:32768
	ds_add_f64 v220, v[202:203] offset:33280
	ds_add_f64 v220, v[204:205] offset:33792
	ds_add_f64 v220, v[206:207] offset:34304
	s_branch .Lg_alldone
.Lg0_A8_flush0:
	v_add_u32_e32 v220, s50, v219
	ds_add_f64 v220, v[200:201] offset:32768
	ds_add_f64 v220, v[202:203] offset:33280
	ds_add_f64 v220, v[204:205] offset:33792
	ds_add_f64 v220, v[206:207] offset:34304
	v_mov_b32_e32 v200, 0
	v_mov_b32_e32 v201, 0
	v_mov_b32_e32 v202, 0
	v_mov_b32_e32 v203, 0
	v_mov_b32_e32 v204, 0
	v_mov_b32_e32 v205, 0
	v_mov_b32_e32 v206, 0
	v_mov_b32_e32 v207, 0
	s_mov_b32 s50, s60
	s_branch .Lg0_A8_cont0

.Lg0_B8_flush13:
	v_add_u32_e32 v220, s50, v219
	ds_add_f64 v220, v[200:201] offset:32768
	ds_add_f64 v220, v[202:203] offset:33280
	ds_add_f64 v220, v[204:205] offset:33792
	ds_add_f64 v220, v[206:207] offset:34304
	v_mov_b32_e32 v200, 0
	v_mov_b32_e32 v201, 0
	v_mov_b32_e32 v202, 0
	v_mov_b32_e32 v203, 0
	v_mov_b32_e32 v204, 0
	v_mov_b32_e32 v205, 0
	v_mov_b32_e32 v206, 0
	v_mov_b32_e32 v207, 0
	s_mov_b32 s50, s73
	s_branch .Lg0_B8_cont13
.Lg0_A0_flush0:
	v_add_u32_e32 v220, s50, v219
	ds_add_f64 v220, v[200:201] offset:32768
	ds_add_f64 v220, v[202:203] offset:33280
	ds_add_f64 v220, v[204:205] offset:33792
	ds_add_f64 v220, v[206:207] offset:34304
	v_mov_b32_e32 v200, 0
	v_mov_b32_e32 v201, 0
	v_mov_b32_e32 v202, 0
	v_mov_b32_e32 v203, 0
	v_mov_b32_e32 v204, 0
	v_mov_b32_e32 v205, 0
	v_mov_b32_e32 v206, 0
	v_mov_b32_e32 v207, 0
	s_mov_b32 s50, s60
	s_branch .Lg0_A0_cont0

.Lg1_start:
	s_add_i32 s53, s8, 7
	s_lshr_b32 s53, s53, 3
	s_mov_b32 s54, s17
	s_add_i32 s55, s17, 4
	s_cmp_ge_u32 s54, s53
	s_cbranch_scc1 .Lg_alldone
	s_mul_i32 s46, s54, 8
	v_add_u32_e32 v220, s46, v221
	v_cmp_gt_u32_e32 vcc, s8, v220
	v_lshlrev_b32_e32 v220, 2, v220
	ds_read_b32 v216, v220
	s_waitcnt lgkmcnt(0)
	v_cndmask_b32_e32 v216, v199, v216, vcc
	s_nop 1
	v_readlane_b32 s50, v216, 0
	s_and_b32 s50, s50, 0xffff
	v_readlane_b32 s40, v216, 0
	s_and_b32 s60, s40, 0xffff
	s_bitcmp1_b32 s40, 31
	s_cselect_b32 s60, 0xffff, s60
	s_bfe_u32 s40, s40, 0xd0010
	s_lshl_b32 s40, s40, 10
	s_add_u32 s42, s32, s40
	s_addc_u32 s43, s33, 0
	global_load_dwordx4 v[66:69], v218, s[42:43] nt
	v_readlane_b32 s40, v216, 1
	s_and_b32 s61, s40, 0xffff
	s_bitcmp1_b32 s40, 31
	s_cselect_b32 s61, 0xffff, s61
	s_bfe_u32 s40, s40, 0xd0010
	s_lshl_b32 s40, s40, 10
	s_add_u32 s42, s32, s40
	s_addc_u32 s43, s33, 0
	global_load_dwordx4 v[70:73], v218, s[42:43] nt
	v_readlane_b32 s40, v216, 2
	s_and_b32 s62, s40, 0xffff
	s_bitcmp1_b32 s40, 31
	s_cselect_b32 s62, 0xffff, s62
	s_bfe_u32 s40, s40, 0xd0010
	s_lshl_b32 s40, s40, 10
	s_add_u32 s42, s32, s40
	s_addc_u32 s43, s33, 0
	global_load_dwordx4 v[74:77], v218, s[42:43] nt
	v_readlane_b32 s40, v216, 3
	s_and_b32 s63, s40, 0xffff
	s_bitcmp1_b32 s40, 31
	s_cselect_b32 s63, 0xffff, s63
	s_bfe_u32 s40, s40, 0xd0010
	s_lshl_b32 s40, s40, 10
	s_add_u32 s42, s32, s40
	s_addc_u32 s43, s33, 0
	global_load_dwordx4 v[78:81], v218, s[42:43] nt
	v_readlane_b32 s40, v216, 4
	s_and_b32 s64, s40, 0xffff
	s_bitcmp1_b32 s40, 31
	s_cselect_b32 s64, 0xffff, s64
	s_bfe_u32 s40, s40, 0xd0010
	s_lshl_b32 s40, s40, 10
	s_add_u32 s42, s32, s40
	s_addc_u32 s43, s33, 0
	global_load_dwordx4 v[82:85], v218, s[42:43] nt
	v_readlane_b32 s40, v216, 5
	s_and_b32 s65, s40, 0xffff
	s_bitcmp1_b32 s40, 31
	s_cselect_b32 s65, 0xffff, s65
	s_bfe_u32 s40, s40, 0xd0010
	s_lshl_b32 s40, s40, 10
	s_add_u32 s42, s32, s40
	s_addc_u32 s43, s33, 0
	global_load_dwordx4 v[86:89], v218, s[42:43] nt
	v_readlane_b32 s40, v216, 6
	s_and_b32 s66, s40, 0xffff
	s_bitcmp1_b32 s40, 31
	s_cselect_b32 s66, 0xffff, s66
	s_bfe_u32 s40, s40, 0xd0010
	s_lshl_b32 s40, s40, 10
	s_add_u32 s42, s32, s40
	s_addc_u32 s43, s33, 0
	global_load_dwordx4 v[90:93], v218, s[42:43] nt
	v_readlane_b32 s40, v216, 7
	s_and_b32 s67, s40, 0xffff
	s_bitcmp1_b32 s40, 31
	s_cselect_b32 s67, 0xffff, s67
	s_bfe_u32 s40, s40, 0xd0010
	s_lshl_b32 s40, s40, 10
	s_add_u32 s42, s32, s40
	s_addc_u32 s43, s33, 0
	global_load_dwordx4 v[94:97], v218, s[42:43] nt
	s_cmp_ge_u32 s55, s53
	s_cbranch_scc1 .Lg1_drainA
	s_mul_i32 s46, s55, 8
	v_add_u32_e32 v220, s46, v221
	v_cmp_gt_u32_e32 vcc, s8, v220
	v_lshlrev_b32_e32 v220, 2, v220
	ds_read_b32 v217, v220
	s_waitcnt lgkmcnt(0)
	v_cndmask_b32_e32 v217, v199, v217, vcc
	s_nop 1
	v_readlane_b32 s40, v217, 0
	s_and_b32 s68, s40, 0xffff
	s_bitcmp1_b32 s40, 31
	s_cselect_b32 s68, 0xffff, s68
	s_bfe_u32 s40, s40, 0xd0010
	s_lshl_b32 s40, s40, 10
	s_add_u32 s42, s32, s40
	s_addc_u32 s43, s33, 0
	global_load_dwordx4 v[98:101], v218, s[42:43] nt
	v_readlane_b32 s40, v217, 1
	s_and_b32 s69, s40, 0xffff
	s_bitcmp1_b32 s40, 31
	s_cselect_b32 s69, 0xffff, s69
	s_bfe_u32 s40, s40, 0xd0010
	s_lshl_b32 s40, s40, 10
	s_add_u32 s42, s32, s40
	s_addc_u32 s43, s33, 0
	global_load_dwordx4 v[102:105], v218, s[42:43] nt
	v_readlane_b32 s40, v217, 2
	s_and_b32 s70, s40, 0xffff
	s_bitcmp1_b32 s40, 31
	s_cselect_b32 s70, 0xffff, s70
	s_bfe_u32 s40, s40, 0xd0010
	s_lshl_b32 s40, s40, 10
	s_add_u32 s42, s32, s40
	s_addc_u32 s43, s33, 0
	global_load_dwordx4 v[106:109], v218, s[42:43] nt
	v_readlane_b32 s40, v217, 3
	s_and_b32 s71, s40, 0xffff
	s_bitcmp1_b32 s40, 31
	s_cselect_b32 s71, 0xffff, s71
	s_bfe_u32 s40, s40, 0xd0010
	s_lshl_b32 s40, s40, 10
	s_add_u32 s42, s32, s40
	s_addc_u32 s43, s33, 0
	global_load_dwordx4 v[110:113], v218, s[42:43] nt
	v_readlane_b32 s40, v217, 4
	s_and_b32 s72, s40, 0xffff
	s_bitcmp1_b32 s40, 31
	s_cselect_b32 s72, 0xffff, s72
	s_bfe_u32 s40, s40, 0xd0010
	s_lshl_b32 s40, s40, 10
	s_add_u32 s42, s32, s40
	s_addc_u32 s43, s33, 0
	global_load_dwordx4 v[114:117], v218, s[42:43] nt
	v_readlane_b32 s40, v217, 5
	s_and_b32 s73, s40, 0xffff
	s_bitcmp1_b32 s40, 31
	s_cselect_b32 s73, 0xffff, s73
	s_bfe_u32 s40, s40, 0xd0010
	s_lshl_b32 s40, s40, 10
	s_add_u32 s42, s32, s40
	s_addc_u32 s43, s33, 0
	global_load_dwordx4 v[118:121], v218, s[42:43] nt
	v_readlane_b32 s40, v217, 6
	s_and_b32 s74, s40, 0xffff
	s_bitcmp1_b32 s40, 31
	s_cselect_b32 s74, 0xffff, s74
	s_bfe_u32 s40, s40, 0xd0010
	s_lshl_b32 s40, s40, 10
	s_add_u32 s42, s32, s40
	s_addc_u32 s43, s33, 0
	global_load_dwordx4 v[122:125], v218, s[42:43] nt
	v_readlane_b32 s40, v217, 7
	s_and_b32 s75, s40, 0xffff
	s_bitcmp1_b32 s40, 31
	s_cselect_b32 s75, 0xffff, s75
	s_bfe_u32 s40, s40, 0xd0010
	s_lshl_b32 s40, s40, 10
	s_add_u32 s42, s32, s40
	s_addc_u32 s43, s33, 0
	global_load_dwordx4 v[126:129], v218, s[42:43] nt
.Lg1_loop:
	s_mov_b64 exec, 1
	ds_add_rtn_u32 v222, v223, v198
	s_mov_b64 exec, -1
	s_waitcnt vmcnt(15)
	s_cmp_eq_u32 s60, 0xffff
	s_cbranch_scc1 .Lg1_A8_skip0
	s_cmp_lg_u32 s60, s50
	s_cbranch_scc1 .Lg1_A8_flush0

.Lg1_A8_skip7:
	s_waitcnt lgkmcnt(0)
	v_readfirstlane_b32 s54, v222
	s_cmp_ge_u32 s54, s53
	s_cbranch_scc1 .Lg1_drainB
	s_mul_i32 s46, s54, 8
	v_add_u32_e32 v220, s46, v221
	v_cmp_gt_u32_e32 vcc, s8, v220
	v_lshlrev_b32_e32 v220, 2, v220
	ds_read_b32 v216, v220
	s_waitcnt lgkmcnt(0)
	v_cndmask_b32_e32 v216, v199, v216, vcc
	s_nop 1
	v_readlane_b32 s40, v216, 0
	s_and_b32 s60, s40, 0xffff
	s_bitcmp1_b32 s40, 31
	s_cselect_b32 s60, 0xffff, s60
	s_bfe_u32 s40, s40, 0xd0010
	s_lshl_b32 s40, s40, 10
	s_add_u32 s42, s32, s40
	s_addc_u32 s43, s33, 0
	global_load_dwordx4 v[66:69], v218, s[42:43] nt
	v_readlane_b32 s40, v216, 1
	s_and_b32 s61, s40, 0xffff
	s_bitcmp1_b32 s40, 31
	s_cselect_b32 s61, 0xffff, s61
	s_bfe_u32 s40, s40, 0xd0010
	s_lshl_b32 s40, s40, 10
	s_add_u32 s42, s32, s40
	s_addc_u32 s43, s33, 0
	global_load_dwordx4 v[70:73], v218, s[42:43] nt
	v_readlane_b32 s40, v216, 2
	s_and_b32 s62, s40, 0xffff
	s_bitcmp1_b32 s40, 31
	s_cselect_b32 s62, 0xffff, s62
	s_bfe_u32 s40, s40, 0xd0010
	s_lshl_b32 s40, s40, 10
	s_add_u32 s42, s32, s40
	s_addc_u32 s43, s33, 0
	global_load_dwordx4 v[74:77], v218, s[42:43] nt
	v_readlane_b32 s40, v216, 3
	s_and_b32 s63, s40, 0xffff
	s_bitcmp1_b32 s40, 31
	s_cselect_b32 s63, 0xffff, s63
	s_bfe_u32 s40, s40, 0xd0010
	s_lshl_b32 s40, s40, 10
	s_add_u32 s42, s32, s40
	s_addc_u32 s43, s33, 0
	global_load_dwordx4 v[78:81], v218, s[42:43] nt
	v_readlane_b32 s40, v216, 4
	s_and_b32 s64, s40, 0xffff
	s_bitcmp1_b32 s40, 31
	s_cselect_b32 s64, 0xffff, s64
	s_bfe_u32 s40, s40, 0xd0010
	s_lshl_b32 s40, s40, 10
	s_add_u32 s42, s32, s40
	s_addc_u32 s43, s33, 0
	global_load_dwordx4 v[82:85], v218, s[42:43] nt
	v_readlane_b32 s40, v216, 5
	s_and_b32 s65, s40, 0xffff
	s_bitcmp1_b32 s40, 31
	s_cselect_b32 s65, 0xffff, s65
	s_bfe_u32 s40, s40, 0xd0010
	s_lshl_b32 s40, s40, 10
	s_add_u32 s42, s32, s40
	s_addc_u32 s43, s33, 0
	global_load_dwordx4 v[86:89], v218, s[42:43] nt
	v_readlane_b32 s40, v216, 6
	s_and_b32 s66, s40, 0xffff
	s_bitcmp1_b32 s40, 31
	s_cselect_b32 s66, 0xffff, s66
	s_bfe_u32 s40, s40, 0xd0010
	s_lshl_b32 s40, s40, 10
	s_add_u32 s42, s32, s40
	s_addc_u32 s43, s33, 0
	global_load_dwordx4 v[90:93], v218, s[42:43] nt
	v_readlane_b32 s40, v216, 7
	s_and_b32 s67, s40, 0xffff
	s_bitcmp1_b32 s40, 31
	s_cselect_b32 s67, 0xffff, s67
	s_bfe_u32 s40, s40, 0xd0010
	s_lshl_b32 s40, s40, 10
	s_add_u32 s42, s32, s40
	s_addc_u32 s43, s33, 0
	global_load_dwordx4 v[94:97], v218, s[42:43] nt
	s_mov_b64 exec, 1
	ds_add_rtn_u32 v222, v223, v198
	s_mov_b64 exec, -1
	s_waitcnt vmcnt(15)
	s_cmp_eq_u32 s68, 0xffff
	s_cbranch_scc1 .Lg1_B8_skip8
	s_cmp_lg_u32 s68, s50
	s_cbranch_scc1 .Lg1_B8_flush8

.Lg1_B8_skip15:
	s_waitcnt lgkmcnt(0)
	v_readfirstlane_b32 s55, v222
	s_cmp_ge_u32 s55, s53
	s_cbranch_scc1 .Lg1_drainA
	s_mul_i32 s46, s55, 8
	v_add_u32_e32 v220, s46, v221
	v_cmp_gt_u32_e32 vcc, s8, v220
	v_lshlrev_b32_e32 v220, 2, v220
	ds_read_b32 v217, v220
	s_waitcnt lgkmcnt(0)
	v_cndmask_b32_e32 v217, v199, v217, vcc
	s_nop 1
	v_readlane_b32 s40, v217, 0
	s_and_b32 s68, s40, 0xffff
	s_bitcmp1_b32 s40, 31
	s_cselect_b32 s68, 0xffff, s68
	s_bfe_u32 s40, s40, 0xd0010
	s_lshl_b32 s40, s40, 10
	s_add_u32 s42, s32, s40
	s_addc_u32 s43, s33, 0
	global_load_dwordx4 v[98:101], v218, s[42:43] nt
	v_readlane_b32 s40, v217, 1
	s_and_b32 s69, s40, 0xffff
	s_bitcmp1_b32 s40, 31
	s_cselect_b32 s69, 0xffff, s69
	s_bfe_u32 s40, s40, 0xd0010
	s_lshl_b32 s40, s40, 10
	s_add_u32 s42, s32, s40
	s_addc_u32 s43, s33, 0
	global_load_dwordx4 v[102:105], v218, s[42:43] nt
	v_readlane_b32 s40, v217, 2
	s_and_b32 s70, s40, 0xffff
	s_bitcmp1_b32 s40, 31
	s_cselect_b32 s70, 0xffff, s70
	s_bfe_u32 s40, s40, 0xd0010
	s_lshl_b32 s40, s40, 10
	s_add_u32 s42, s32, s40
	s_addc_u32 s43, s33, 0
	global_load_dwordx4 v[106:109], v218, s[42:43] nt
	v_readlane_b32 s40, v217, 3
	s_and_b32 s71, s40, 0xffff
	s_bitcmp1_b32 s40, 31
	s_cselect_b32 s71, 0xffff, s71
	s_bfe_u32 s40, s40, 0xd0010
	s_lshl_b32 s40, s40, 10
	s_add_u32 s42, s32, s40
	s_addc_u32 s43, s33, 0
	global_load_dwordx4 v[110:113], v218, s[42:43] nt
	v_readlane_b32 s40, v217, 4
	s_and_b32 s72, s40, 0xffff
	s_bitcmp1_b32 s40, 31
	s_cselect_b32 s72, 0xffff, s72
	s_bfe_u32 s40, s40, 0xd0010
	s_lshl_b32 s40, s40, 10
	s_add_u32 s42, s32, s40
	s_addc_u32 s43, s33, 0
	global_load_dwordx4 v[114:117], v218, s[42:43] nt
	v_readlane_b32 s40, v217, 5
	s_and_b32 s73, s40, 0xffff
	s_bitcmp1_b32 s40, 31
	s_cselect_b32 s73, 0xffff, s73
	s_bfe_u32 s40, s40, 0xd0010
	s_lshl_b32 s40, s40, 10
	s_add_u32 s42, s32, s40
	s_addc_u32 s43, s33, 0
	global_load_dwordx4 v[118:121], v218, s[42:43] nt
	v_readlane_b32 s40, v217, 6
	s_and_b32 s74, s40, 0xffff
	s_bitcmp1_b32 s40, 31
	s_cselect_b32 s74, 0xffff, s74
	s_bfe_u32 s40, s40, 0xd0010
	s_lshl_b32 s40, s40, 10
	s_add_u32 s42, s32, s40
	s_addc_u32 s43, s33, 0
	global_load_dwordx4 v[122:125], v218, s[42:43] nt
	v_readlane_b32 s40, v217, 7
	s_and_b32 s75, s40, 0xffff
	s_bitcmp1_b32 s40, 31
	s_cselect_b32 s75, 0xffff, s75
	s_bfe_u32 s40, s40, 0xd0010
	s_lshl_b32 s40, s40, 10
	s_add_u32 s42, s32, s40
	s_addc_u32 s43, s33, 0
	global_load_dwordx4 v[126:129], v218, s[42:43] nt
	s_branch .Lg1_loop

.Lg1_B0_skip15:
.Lg1_fin:
	v_add_u32_e32 v220, s50, v219
	ds_add_f64 v220, v[200:201] offset:32768
	ds_add_f64 v220, v[202:203] offset:33280
	ds_add_f64 v220, v[204:205] offset:33792
	ds_add_f64 v220, v[206:207] offset:34304
	s_branch .Lg_alldone
.Lg1_A8_flush0:
	v_add_u32_e32 v220, s50, v219
	ds_add_f64 v220, v[200:201] offset:32768
	ds_add_f64 v220, v[202:203] offset:33280
	ds_add_f64 v220, v[204:205] offset:33792
	ds_add_f64 v220, v[206:207] offset:34304
	v_mov_b32_e32 v200, 0
	v_mov_b32_e32 v201, 0
	v_mov_b32_e32 v202, 0
	v_mov_b32_e32 v203, 0
	v_mov_b32_e32 v204, 0
	v_mov_b32_e32 v205, 0
	v_mov_b32_e32 v206, 0
	v_mov_b32_e32 v207, 0
	s_mov_b32 s50, s60
	s_branch .Lg1_A8_cont0

.Lg2_start:
	s_add_i32 s53, s8, 8
	s_mul_hi_u32 s53, s53, 0xe38e38e4
	s_lshr_b32 s53, s53, 3
	s_mov_b32 s54, s17
	s_add_i32 s55, s17, 4
	s_cmp_ge_u32 s54, s53
	s_cbranch_scc1 .Lg_alldone
	s_mul_i32 s46, s54, 9
	v_add_u32_e32 v220, s46, v221
	v_cmp_gt_u32_e32 vcc, s8, v220
	v_lshlrev_b32_e32 v220, 2, v220
	ds_read_b32 v216, v220
	s_waitcnt lgkmcnt(0)
	v_cndmask_b32_e32 v216, v199, v216, vcc
	s_nop 1
	v_readlane_b32 s50, v216, 0
	s_and_b32 s50, s50, 0xffff
	v_readlane_b32 s40, v216, 0
	s_and_b32 s60, s40, 0xffff
	s_bitcmp1_b32 s40, 31
	s_cselect_b32 s60, 0xffff, s60
	s_bfe_u32 s40, s40, 0xd0010
	s_lshl_b32 s40, s40, 10
	s_add_u32 s42, s32, s40
	s_addc_u32 s43, s33, 0
	global_load_dwordx4 v[66:69], v218, s[42:43] nt
	v_readlane_b32 s40, v216, 1
	s_and_b32 s61, s40, 0xffff
	s_bitcmp1_b32 s40, 31
	s_cselect_b32 s61, 0xffff, s61
	s_bfe_u32 s40, s40, 0xd0010
	s_lshl_b32 s40, s40, 10
	s_add_u32 s42, s32, s40
	s_addc_u32 s43, s33, 0
	global_load_dwordx4 v[70:73], v218, s[42:43] nt
	v_readlane_b32 s40, v216, 2
	s_and_b32 s62, s40, 0xffff
	s_bitcmp1_b32 s40, 31
	s_cselect_b32 s62, 0xffff, s62
	s_bfe_u32 s40, s40, 0xd0010
	s_lshl_b32 s40, s40, 10
	s_add_u32 s42, s32, s40
	s_addc_u32 s43, s33, 0
	global_load_dwordx4 v[74:77], v218, s[42:43] nt
	v_readlane_b32 s40, v216, 3
	s_and_b32 s63, s40, 0xffff
	s_bitcmp1_b32 s40, 31
	s_cselect_b32 s63, 0xffff, s63
	s_bfe_u32 s40, s40, 0xd0010
	s_lshl_b32 s40, s40, 10
	s_add_u32 s42, s32, s40
	s_addc_u32 s43, s33, 0
	global_load_dwordx4 v[78:81], v218, s[42:43] nt
	v_readlane_b32 s40, v216, 4
	s_and_b32 s64, s40, 0xffff
	s_bitcmp1_b32 s40, 31
	s_cselect_b32 s64, 0xffff, s64
	s_bfe_u32 s40, s40, 0xd0010
	s_lshl_b32 s40, s40, 10
	s_add_u32 s42, s32, s40
	s_addc_u32 s43, s33, 0
	global_load_dwordx4 v[82:85], v218, s[42:43] nt
	v_readlane_b32 s40, v216, 5
	s_and_b32 s65, s40, 0xffff
	s_bitcmp1_b32 s40, 31
	s_cselect_b32 s65, 0xffff, s65
	s_bfe_u32 s40, s40, 0xd0010
	s_lshl_b32 s40, s40, 10
	s_add_u32 s42, s32, s40
	s_addc_u32 s43, s33, 0
	global_load_dwordx4 v[86:89], v218, s[42:43] nt
	v_readlane_b32 s40, v216, 6
	s_and_b32 s66, s40, 0xffff
	s_bitcmp1_b32 s40, 31
	s_cselect_b32 s66, 0xffff, s66
	s_bfe_u32 s40, s40, 0xd0010
	s_lshl_b32 s40, s40, 10
	s_add_u32 s42, s32, s40
	s_addc_u32 s43, s33, 0
	global_load_dwordx4 v[90:93], v218, s[42:43] nt
	v_readlane_b32 s40, v216, 7
	s_and_b32 s67, s40, 0xffff
	s_bitcmp1_b32 s40, 31
	s_cselect_b32 s67, 0xffff, s67
	s_bfe_u32 s40, s40, 0xd0010
	s_lshl_b32 s40, s40, 10
	s_add_u32 s42, s32, s40
	s_addc_u32 s43, s33, 0
	global_load_dwordx4 v[94:97], v218, s[42:43] nt
	v_readlane_b32 s40, v216, 8
	s_and_b32 s68, s40, 0xffff
	s_bitcmp1_b32 s40, 31
	s_cselect_b32 s68, 0xffff, s68
	s_bfe_u32 s40, s40, 0xd0010
	s_lshl_b32 s40, s40, 10
	s_add_u32 s42, s32, s40
	s_addc_u32 s43, s33, 0
	global_load_dwordx4 v[98:101], v218, s[42:43] nt
	s_cmp_ge_u32 s55, s53
	s_cbranch_scc1 .Lg2_drainA
	s_mul_i32 s46, s55, 9
	v_add_u32_e32 v220, s46, v221
	v_cmp_gt_u32_e32 vcc, s8, v220
	v_lshlrev_b32_e32 v220, 2, v220
	ds_read_b32 v217, v220
	s_waitcnt lgkmcnt(0)
	v_cndmask_b32_e32 v217, v199, v217, vcc
	s_nop 1
	v_readlane_b32 s40, v217, 0
	s_and_b32 s69, s40, 0xffff
	s_bitcmp1_b32 s40, 31
	s_cselect_b32 s69, 0xffff, s69
	s_bfe_u32 s40, s40, 0xd0010
	s_lshl_b32 s40, s40, 10
	s_add_u32 s42, s32, s40
	s_addc_u32 s43, s33, 0
	global_load_dwordx4 v[102:105], v218, s[42:43] nt
	v_readlane_b32 s40, v217, 1
	s_and_b32 s70, s40, 0xffff
	s_bitcmp1_b32 s40, 31
	s_cselect_b32 s70, 0xffff, s70
	s_bfe_u32 s40, s40, 0xd0010
	s_lshl_b32 s40, s40, 10
	s_add_u32 s42, s32, s40
	s_addc_u32 s43, s33, 0
	global_load_dwordx4 v[106:109], v218, s[42:43] nt
	v_readlane_b32 s40, v217, 2
	s_and_b32 s71, s40, 0xffff
	s_bitcmp1_b32 s40, 31
	s_cselect_b32 s71, 0xffff, s71
	s_bfe_u32 s40, s40, 0xd0010
	s_lshl_b32 s40, s40, 10
	s_add_u32 s42, s32, s40
	s_addc_u32 s43, s33, 0
	global_load_dwordx4 v[110:113], v218, s[42:43] nt
	v_readlane_b32 s40, v217, 3
	s_and_b32 s72, s40, 0xffff
	s_bitcmp1_b32 s40, 31
	s_cselect_b32 s72, 0xffff, s72
	s_bfe_u32 s40, s40, 0xd0010
	s_lshl_b32 s40, s40, 10
	s_add_u32 s42, s32, s40
	s_addc_u32 s43, s33, 0
	global_load_dwordx4 v[114:117], v218, s[42:43] nt
	v_readlane_b32 s40, v217, 4
	s_and_b32 s73, s40, 0xffff
	s_bitcmp1_b32 s40, 31
	s_cselect_b32 s73, 0xffff, s73
	s_bfe_u32 s40, s40, 0xd0010
	s_lshl_b32 s40, s40, 10
	s_add_u32 s42, s32, s40
	s_addc_u32 s43, s33, 0
	global_load_dwordx4 v[118:121], v218, s[42:43] nt
	v_readlane_b32 s40, v217, 5
	s_and_b32 s74, s40, 0xffff
	s_bitcmp1_b32 s40, 31
	s_cselect_b32 s74, 0xffff, s74
	s_bfe_u32 s40, s40, 0xd0010
	s_lshl_b32 s40, s40, 10
	s_add_u32 s42, s32, s40
	s_addc_u32 s43, s33, 0
	global_load_dwordx4 v[122:125], v218, s[42:43] nt
	v_readlane_b32 s40, v217, 6
	s_and_b32 s75, s40, 0xffff
	s_bitcmp1_b32 s40, 31
	s_cselect_b32 s75, 0xffff, s75
	s_bfe_u32 s40, s40, 0xd0010
	s_lshl_b32 s40, s40, 10
	s_add_u32 s42, s32, s40
	s_addc_u32 s43, s33, 0
	global_load_dwordx4 v[126:129], v218, s[42:43] nt
	v_readlane_b32 s40, v217, 7
	s_and_b32 s76, s40, 0xffff
	s_bitcmp1_b32 s40, 31
	s_cselect_b32 s76, 0xffff, s76
	s_bfe_u32 s40, s40, 0xd0010
	s_lshl_b32 s40, s40, 10
	s_add_u32 s42, s32, s40
	s_addc_u32 s43, s33, 0
	global_load_dwordx4 v[130:133], v218, s[42:43] nt
	v_readlane_b32 s40, v217, 8
	s_and_b32 s77, s40, 0xffff
	s_bitcmp1_b32 s40, 31
	s_cselect_b32 s77, 0xffff, s77
	s_bfe_u32 s40, s40, 0xd0010
	s_lshl_b32 s40, s40, 10
	s_add_u32 s42, s32, s40
	s_addc_u32 s43, s33, 0
	global_load_dwordx4 v[134:137], v218, s[42:43] nt
.Lg2_loop:
	s_mov_b64 exec, 1
	ds_add_rtn_u32 v222, v223, v198
	s_mov_b64 exec, -1
	s_waitcnt vmcnt(17)
	s_cmp_eq_u32 s60, 0xffff
	s_cbranch_scc1 .Lg2_A8_skip0
	s_cmp_lg_u32 s60, s50
	s_cbranch_scc1 .Lg2_A8_flush0

.Lg2_A8_skip0:
	s_waitcnt vmcnt(16)
	s_cmp_eq_u32 s61, 0xffff
	s_cbranch_scc1 .Lg2_A8_skip1
	s_cmp_lg_u32 s61, s50
	s_cbranch_scc1 .Lg2_A8_flush1

.Lg2_A8_skip1:
	s_waitcnt vmcnt(15)
	s_cmp_eq_u32 s62, 0xffff
	s_cbranch_scc1 .Lg2_A8_skip2
	s_cmp_lg_u32 s62, s50
	s_cbranch_scc1 .Lg2_A8_flush2

.Lg2_A8_skip2:
	s_waitcnt vmcnt(14)
	s_cmp_eq_u32 s63, 0xffff
	s_cbranch_scc1 .Lg2_A8_skip3
	s_cmp_lg_u32 s63, s50
	s_cbranch_scc1 .Lg2_A8_flush3

.Lg2_A8_skip3:
	s_waitcnt vmcnt(13)
	s_cmp_eq_u32 s64, 0xffff
	s_cbranch_scc1 .Lg2_A8_skip4
	s_cmp_lg_u32 s64, s50
	s_cbranch_scc1 .Lg2_A8_flush4

.Lg2_A8_skip4:
	s_waitcnt vmcnt(12)
	s_cmp_eq_u32 s65, 0xffff
	s_cbranch_scc1 .Lg2_A8_skip5
	s_cmp_lg_u32 s65, s50
	s_cbranch_scc1 .Lg2_A8_flush5

.Lg2_A8_skip5:
	s_waitcnt vmcnt(11)
	s_cmp_eq_u32 s66, 0xffff
	s_cbranch_scc1 .Lg2_A8_skip6
	s_cmp_lg_u32 s66, s50
	s_cbranch_scc1 .Lg2_A8_flush6

.Lg2_A8_skip6:
	s_waitcnt vmcnt(10)
	s_cmp_eq_u32 s67, 0xffff
	s_cbranch_scc1 .Lg2_A8_skip7
	s_cmp_lg_u32 s67, s50
	s_cbranch_scc1 .Lg2_A8_flush7

.Lg2_A8_skip7:
	s_waitcnt vmcnt(9)
	s_cmp_eq_u32 s68, 0xffff
	s_cbranch_scc1 .Lg2_A8_skip8
	s_cmp_lg_u32 s68, s50
	s_cbranch_scc1 .Lg2_A8_flush8

.Lg2_A8_skip8:
	s_waitcnt lgkmcnt(0)
	v_readfirstlane_b32 s54, v222
	s_cmp_ge_u32 s54, s53
	s_cbranch_scc1 .Lg2_drainB
	s_mul_i32 s46, s54, 9
	v_add_u32_e32 v220, s46, v221
	v_cmp_gt_u32_e32 vcc, s8, v220
	v_lshlrev_b32_e32 v220, 2, v220
	ds_read_b32 v216, v220
	s_waitcnt lgkmcnt(0)
	v_cndmask_b32_e32 v216, v199, v216, vcc
	s_nop 1
	v_readlane_b32 s40, v216, 0
	s_and_b32 s60, s40, 0xffff
	s_bitcmp1_b32 s40, 31
	s_cselect_b32 s60, 0xffff, s60
	s_bfe_u32 s40, s40, 0xd0010
	s_lshl_b32 s40, s40, 10
	s_add_u32 s42, s32, s40
	s_addc_u32 s43, s33, 0
	global_load_dwordx4 v[66:69], v218, s[42:43] nt
	v_readlane_b32 s40, v216, 1
	s_and_b32 s61, s40, 0xffff
	s_bitcmp1_b32 s40, 31
	s_cselect_b32 s61, 0xffff, s61
	s_bfe_u32 s40, s40, 0xd0010
	s_lshl_b32 s40, s40, 10
	s_add_u32 s42, s32, s40
	s_addc_u32 s43, s33, 0
	global_load_dwordx4 v[70:73], v218, s[42:43] nt
	v_readlane_b32 s40, v216, 2
	s_and_b32 s62, s40, 0xffff
	s_bitcmp1_b32 s40, 31
	s_cselect_b32 s62, 0xffff, s62
	s_bfe_u32 s40, s40, 0xd0010
	s_lshl_b32 s40, s40, 10
	s_add_u32 s42, s32, s40
	s_addc_u32 s43, s33, 0
	global_load_dwordx4 v[74:77], v218, s[42:43] nt
	v_readlane_b32 s40, v216, 3
	s_and_b32 s63, s40, 0xffff
	s_bitcmp1_b32 s40, 31
	s_cselect_b32 s63, 0xffff, s63
	s_bfe_u32 s40, s40, 0xd0010
	s_lshl_b32 s40, s40, 10
	s_add_u32 s42, s32, s40
	s_addc_u32 s43, s33, 0
	global_load_dwordx4 v[78:81], v218, s[42:43] nt
	v_readlane_b32 s40, v216, 4
	s_and_b32 s64, s40, 0xffff
	s_bitcmp1_b32 s40, 31
	s_cselect_b32 s64, 0xffff, s64
	s_bfe_u32 s40, s40, 0xd0010
	s_lshl_b32 s40, s40, 10
	s_add_u32 s42, s32, s40
	s_addc_u32 s43, s33, 0
	global_load_dwordx4 v[82:85], v218, s[42:43] nt
	v_readlane_b32 s40, v216, 5
	s_and_b32 s65, s40, 0xffff
	s_bitcmp1_b32 s40, 31
	s_cselect_b32 s65, 0xffff, s65
	s_bfe_u32 s40, s40, 0xd0010
	s_lshl_b32 s40, s40, 10
	s_add_u32 s42, s32, s40
	s_addc_u32 s43, s33, 0
	global_load_dwordx4 v[86:89], v218, s[42:43] nt
	v_readlane_b32 s40, v216, 6
	s_and_b32 s66, s40, 0xffff
	s_bitcmp1_b32 s40, 31
	s_cselect_b32 s66, 0xffff, s66
	s_bfe_u32 s40, s40, 0xd0010
	s_lshl_b32 s40, s40, 10
	s_add_u32 s42, s32, s40
	s_addc_u32 s43, s33, 0
	global_load_dwordx4 v[90:93], v218, s[42:43] nt
	v_readlane_b32 s40, v216, 7
	s_and_b32 s67, s40, 0xffff
	s_bitcmp1_b32 s40, 31
	s_cselect_b32 s67, 0xffff, s67
	s_bfe_u32 s40, s40, 0xd0010
	s_lshl_b32 s40, s40, 10
	s_add_u32 s42, s32, s40
	s_addc_u32 s43, s33, 0
	global_load_dwordx4 v[94:97], v218, s[42:43] nt
	v_readlane_b32 s40, v216, 8
	s_and_b32 s68, s40, 0xffff
	s_bitcmp1_b32 s40, 31
	s_cselect_b32 s68, 0xffff, s68
	s_bfe_u32 s40, s40, 0xd0010
	s_lshl_b32 s40, s40, 10
	s_add_u32 s42, s32, s40
	s_addc_u32 s43, s33, 0
	global_load_dwordx4 v[98:101], v218, s[42:43] nt
	s_mov_b64 exec, 1
	ds_add_rtn_u32 v222, v223, v198
	s_mov_b64 exec, -1
	s_waitcnt vmcnt(17)
	s_cmp_eq_u32 s69, 0xffff
	s_cbranch_scc1 .Lg2_B8_skip9
	s_cmp_lg_u32 s69, s50
	s_cbranch_scc1 .Lg2_B8_flush9

.Lg2_B8_skip9:
	s_waitcnt vmcnt(16)
	s_cmp_eq_u32 s70, 0xffff
	s_cbranch_scc1 .Lg2_B8_skip10
	s_cmp_lg_u32 s70, s50
	s_cbranch_scc1 .Lg2_B8_flush10

.Lg2_B8_skip10:
	s_waitcnt vmcnt(15)
	s_cmp_eq_u32 s71, 0xffff
	s_cbranch_scc1 .Lg2_B8_skip11
	s_cmp_lg_u32 s71, s50
	s_cbranch_scc1 .Lg2_B8_flush11

.Lg2_B8_skip11:
	s_waitcnt vmcnt(14)
	s_cmp_eq_u32 s72, 0xffff
	s_cbranch_scc1 .Lg2_B8_skip12
	s_cmp_lg_u32 s72, s50
	s_cbranch_scc1 .Lg2_B8_flush12

.Lg2_B8_skip12:
	s_waitcnt vmcnt(13)
	s_cmp_eq_u32 s73, 0xffff
	s_cbranch_scc1 .Lg2_B8_skip13
	s_cmp_lg_u32 s73, s50
	s_cbranch_scc1 .Lg2_B8_flush13

.Lg2_B8_skip13:
	s_waitcnt vmcnt(12)
	s_cmp_eq_u32 s74, 0xffff
	s_cbranch_scc1 .Lg2_B8_skip14
	s_cmp_lg_u32 s74, s50
	s_cbranch_scc1 .Lg2_B8_flush14

.Lg2_B8_skip14:
	s_waitcnt vmcnt(11)
	s_cmp_eq_u32 s75, 0xffff
	s_cbranch_scc1 .Lg2_B8_skip15
	s_cmp_lg_u32 s75, s50
	s_cbranch_scc1 .Lg2_B8_flush15

.Lg2_B8_skip15:
	s_waitcnt vmcnt(10)
	s_cmp_eq_u32 s76, 0xffff
	s_cbranch_scc1 .Lg2_B8_skip16
	s_cmp_lg_u32 s76, s50
	s_cbranch_scc1 .Lg2_B8_flush16
.Lg2_B8_cont16:
	v_cvt_f64_f32_e32 v[208:209], v130
	v_cvt_f64_f32_e32 v[210:211], v131
	v_cvt_f64_f32_e32 v[212:213], v132
	v_cvt_f64_f32_e32 v[214:215], v133
	v_add_f64 v[200:201], v[200:201], v[208:209]
	v_add_f64 v[202:203], v[202:203], v[210:211]
	v_add_f64 v[204:205], v[204:205], v[212:213]
	v_add_f64 v[206:207], v[206:207], v[214:215]
.Lg2_B8_skip16:
	s_waitcnt vmcnt(9)
	s_cmp_eq_u32 s77, 0xffff
	s_cbranch_scc1 .Lg2_B8_skip17
	s_cmp_lg_u32 s77, s50
	s_cbranch_scc1 .Lg2_B8_flush17
.Lg2_B8_cont17:
	v_cvt_f64_f32_e32 v[208:209], v134
	v_cvt_f64_f32_e32 v[210:211], v135
	v_cvt_f64_f32_e32 v[212:213], v136
	v_cvt_f64_f32_e32 v[214:215], v137
	v_add_f64 v[200:201], v[200:201], v[208:209]
	v_add_f64 v[202:203], v[202:203], v[210:211]
	v_add_f64 v[204:205], v[204:205], v[212:213]
	v_add_f64 v[206:207], v[206:207], v[214:215]
.Lg2_B8_skip17:
	s_waitcnt lgkmcnt(0)
	v_readfirstlane_b32 s55, v222
	s_cmp_ge_u32 s55, s53
	s_cbranch_scc1 .Lg2_drainA
	s_mul_i32 s46, s55, 9
	v_add_u32_e32 v220, s46, v221
	v_cmp_gt_u32_e32 vcc, s8, v220
	v_lshlrev_b32_e32 v220, 2, v220
	ds_read_b32 v217, v220
	s_waitcnt lgkmcnt(0)
	v_cndmask_b32_e32 v217, v199, v217, vcc
	s_nop 1
	v_readlane_b32 s40, v217, 0
	s_and_b32 s69, s40, 0xffff
	s_bitcmp1_b32 s40, 31
	s_cselect_b32 s69, 0xffff, s69
	s_bfe_u32 s40, s40, 0xd0010
	s_lshl_b32 s40, s40, 10
	s_add_u32 s42, s32, s40
	s_addc_u32 s43, s33, 0
	global_load_dwordx4 v[102:105], v218, s[42:43] nt
	v_readlane_b32 s40, v217, 1
	s_and_b32 s70, s40, 0xffff
	s_bitcmp1_b32 s40, 31
	s_cselect_b32 s70, 0xffff, s70
	s_bfe_u32 s40, s40, 0xd0010
	s_lshl_b32 s40, s40, 10
	s_add_u32 s42, s32, s40
	s_addc_u32 s43, s33, 0
	global_load_dwordx4 v[106:109], v218, s[42:43] nt
	v_readlane_b32 s40, v217, 2
	s_and_b32 s71, s40, 0xffff
	s_bitcmp1_b32 s40, 31
	s_cselect_b32 s71, 0xffff, s71
	s_bfe_u32 s40, s40, 0xd0010
	s_lshl_b32 s40, s40, 10
	s_add_u32 s42, s32, s40
	s_addc_u32 s43, s33, 0
	global_load_dwordx4 v[110:113], v218, s[42:43] nt
	v_readlane_b32 s40, v217, 3
	s_and_b32 s72, s40, 0xffff
	s_bitcmp1_b32 s40, 31
	s_cselect_b32 s72, 0xffff, s72
	s_bfe_u32 s40, s40, 0xd0010
	s_lshl_b32 s40, s40, 10
	s_add_u32 s42, s32, s40
	s_addc_u32 s43, s33, 0
	global_load_dwordx4 v[114:117], v218, s[42:43] nt
	v_readlane_b32 s40, v217, 4
	s_and_b32 s73, s40, 0xffff
	s_bitcmp1_b32 s40, 31
	s_cselect_b32 s73, 0xffff, s73
	s_bfe_u32 s40, s40, 0xd0010
	s_lshl_b32 s40, s40, 10
	s_add_u32 s42, s32, s40
	s_addc_u32 s43, s33, 0
	global_load_dwordx4 v[118:121], v218, s[42:43] nt
	v_readlane_b32 s40, v217, 5
	s_and_b32 s74, s40, 0xffff
	s_bitcmp1_b32 s40, 31
	s_cselect_b32 s74, 0xffff, s74
	s_bfe_u32 s40, s40, 0xd0010
	s_lshl_b32 s40, s40, 10
	s_add_u32 s42, s32, s40
	s_addc_u32 s43, s33, 0
	global_load_dwordx4 v[122:125], v218, s[42:43] nt
	v_readlane_b32 s40, v217, 6
	s_and_b32 s75, s40, 0xffff
	s_bitcmp1_b32 s40, 31
	s_cselect_b32 s75, 0xffff, s75
	s_bfe_u32 s40, s40, 0xd0010
	s_lshl_b32 s40, s40, 10
	s_add_u32 s42, s32, s40
	s_addc_u32 s43, s33, 0
	global_load_dwordx4 v[126:129], v218, s[42:43] nt
	v_readlane_b32 s40, v217, 7
	s_and_b32 s76, s40, 0xffff
	s_bitcmp1_b32 s40, 31
	s_cselect_b32 s76, 0xffff, s76
	s_bfe_u32 s40, s40, 0xd0010
	s_lshl_b32 s40, s40, 10
	s_add_u32 s42, s32, s40
	s_addc_u32 s43, s33, 0
	global_load_dwordx4 v[130:133], v218, s[42:43] nt
	v_readlane_b32 s40, v217, 8
	s_and_b32 s77, s40, 0xffff
	s_bitcmp1_b32 s40, 31
	s_cselect_b32 s77, 0xffff, s77
	s_bfe_u32 s40, s40, 0xd0010
	s_lshl_b32 s40, s40, 10
	s_add_u32 s42, s32, s40
	s_addc_u32 s43, s33, 0
	global_load_dwordx4 v[134:137], v218, s[42:43] nt
	s_branch .Lg2_loop
.Lg2_drainA:
	s_waitcnt vmcnt(8)
	s_cmp_eq_u32 s60, 0xffff
	s_cbranch_scc1 .Lg2_A0_skip0
	s_cmp_lg_u32 s60, s50
	s_cbranch_scc1 .Lg2_A0_flush0

.Lg2_A0_skip0:
	s_waitcnt vmcnt(7)
	s_cmp_eq_u32 s61, 0xffff
	s_cbranch_scc1 .Lg2_A0_skip1
	s_cmp_lg_u32 s61, s50
	s_cbranch_scc1 .Lg2_A0_flush1

.Lg2_A0_skip1:
	s_waitcnt vmcnt(6)
	s_cmp_eq_u32 s62, 0xffff
	s_cbranch_scc1 .Lg2_A0_skip2
	s_cmp_lg_u32 s62, s50
	s_cbranch_scc1 .Lg2_A0_flush2

.Lg2_A0_skip2:
	s_waitcnt vmcnt(5)
	s_cmp_eq_u32 s63, 0xffff
	s_cbranch_scc1 .Lg2_A0_skip3
	s_cmp_lg_u32 s63, s50
	s_cbranch_scc1 .Lg2_A0_flush3

.Lg2_A0_skip3:
	s_waitcnt vmcnt(4)
	s_cmp_eq_u32 s64, 0xffff
	s_cbranch_scc1 .Lg2_A0_skip4
	s_cmp_lg_u32 s64, s50
	s_cbranch_scc1 .Lg2_A0_flush4

.Lg2_A0_skip4:
	s_waitcnt vmcnt(3)
	s_cmp_eq_u32 s65, 0xffff
	s_cbranch_scc1 .Lg2_A0_skip5
	s_cmp_lg_u32 s65, s50
	s_cbranch_scc1 .Lg2_A0_flush5

.Lg2_A0_skip5:
	s_waitcnt vmcnt(2)
	s_cmp_eq_u32 s66, 0xffff
	s_cbranch_scc1 .Lg2_A0_skip6
	s_cmp_lg_u32 s66, s50
	s_cbranch_scc1 .Lg2_A0_flush6

.Lg2_A0_skip6:
	s_waitcnt vmcnt(1)
	s_cmp_eq_u32 s67, 0xffff
	s_cbranch_scc1 .Lg2_A0_skip7
	s_cmp_lg_u32 s67, s50
	s_cbranch_scc1 .Lg2_A0_flush7

.Lg2_A0_skip7:
	s_waitcnt vmcnt(0)
	s_cmp_eq_u32 s68, 0xffff
	s_cbranch_scc1 .Lg2_A0_skip8
	s_cmp_lg_u32 s68, s50
	s_cbranch_scc1 .Lg2_A0_flush8
.Lg2_A0_cont8:
	v_cvt_f64_f32_e32 v[208:209], v98
	v_cvt_f64_f32_e32 v[210:211], v99
	v_cvt_f64_f32_e32 v[212:213], v100
	v_cvt_f64_f32_e32 v[214:215], v101
	v_add_f64 v[200:201], v[200:201], v[208:209]
	v_add_f64 v[202:203], v[202:203], v[210:211]
	v_add_f64 v[204:205], v[204:205], v[212:213]
	v_add_f64 v[206:207], v[206:207], v[214:215]
.Lg2_A0_skip8:
	s_branch .Lg2_fin
.Lg2_drainB:
	s_waitcnt vmcnt(8)
	s_cmp_eq_u32 s69, 0xffff
	s_cbranch_scc1 .Lg2_B0_skip9
	s_cmp_lg_u32 s69, s50
	s_cbranch_scc1 .Lg2_B0_flush9

.Lg2_B0_skip9:
	s_waitcnt vmcnt(7)
	s_cmp_eq_u32 s70, 0xffff
	s_cbranch_scc1 .Lg2_B0_skip10
	s_cmp_lg_u32 s70, s50
	s_cbranch_scc1 .Lg2_B0_flush10

.Lg2_B0_skip10:
	s_waitcnt vmcnt(6)
	s_cmp_eq_u32 s71, 0xffff
	s_cbranch_scc1 .Lg2_B0_skip11
	s_cmp_lg_u32 s71, s50
	s_cbranch_scc1 .Lg2_B0_flush11

.Lg2_B0_skip11:
	s_waitcnt vmcnt(5)
	s_cmp_eq_u32 s72, 0xffff
	s_cbranch_scc1 .Lg2_B0_skip12
	s_cmp_lg_u32 s72, s50
	s_cbranch_scc1 .Lg2_B0_flush12

.Lg2_B0_skip12:
	s_waitcnt vmcnt(4)
	s_cmp_eq_u32 s73, 0xffff
	s_cbranch_scc1 .Lg2_B0_skip13
	s_cmp_lg_u32 s73, s50
	s_cbranch_scc1 .Lg2_B0_flush13

.Lg2_B0_skip13:
	s_waitcnt vmcnt(3)
	s_cmp_eq_u32 s74, 0xffff
	s_cbranch_scc1 .Lg2_B0_skip14
	s_cmp_lg_u32 s74, s50
	s_cbranch_scc1 .Lg2_B0_flush14

.Lg2_B0_skip14:
	s_waitcnt vmcnt(2)
	s_cmp_eq_u32 s75, 0xffff
	s_cbranch_scc1 .Lg2_B0_skip15
	s_cmp_lg_u32 s75, s50
	s_cbranch_scc1 .Lg2_B0_flush15

.Lg2_B0_skip15:
	s_waitcnt vmcnt(1)
	s_cmp_eq_u32 s76, 0xffff
	s_cbranch_scc1 .Lg2_B0_skip16
	s_cmp_lg_u32 s76, s50
	s_cbranch_scc1 .Lg2_B0_flush16

.Lg2_B0_skip16:
	s_waitcnt vmcnt(0)
	s_cmp_eq_u32 s77, 0xffff
	s_cbranch_scc1 .Lg2_B0_skip17
	s_cmp_lg_u32 s77, s50
	s_cbranch_scc1 .Lg2_B0_flush17

.Lg2_B0_skip17:
.Lg2_fin:
	v_add_u32_e32 v220, s50, v219
	ds_add_f64 v220, v[200:201] offset:32768
	ds_add_f64 v220, v[202:203] offset:33280
	ds_add_f64 v220, v[204:205] offset:33792
	ds_add_f64 v220, v[206:207] offset:34304
	s_branch .Lg_alldone
.Lg2_A8_flush0:
	v_add_u32_e32 v220, s50, v219
	ds_add_f64 v220, v[200:201] offset:32768
	ds_add_f64 v220, v[202:203] offset:33280
	ds_add_f64 v220, v[204:205] offset:33792
	ds_add_f64 v220, v[206:207] offset:34304
	v_mov_b32_e32 v200, 0
	v_mov_b32_e32 v201, 0
	v_mov_b32_e32 v202, 0
	v_mov_b32_e32 v203, 0
	v_mov_b32_e32 v204, 0
	v_mov_b32_e32 v205, 0
	v_mov_b32_e32 v206, 0
	v_mov_b32_e32 v207, 0
	s_mov_b32 s50, s60
	s_branch .Lg2_A8_cont0

.Lg2_B8_flush16:
	v_add_u32_e32 v220, s50, v219
	ds_add_f64 v220, v[200:201] offset:32768
	ds_add_f64 v220, v[202:203] offset:33280
	ds_add_f64 v220, v[204:205] offset:33792
	ds_add_f64 v220, v[206:207] offset:34304
	v_mov_b32_e32 v200, 0
	v_mov_b32_e32 v201, 0
	v_mov_b32_e32 v202, 0
	v_mov_b32_e32 v203, 0
	v_mov_b32_e32 v204, 0
	v_mov_b32_e32 v205, 0
	v_mov_b32_e32 v206, 0
	v_mov_b32_e32 v207, 0
	s_mov_b32 s50, s76
	s_branch .Lg2_B8_cont16
.Lg2_B8_flush17:
	v_add_u32_e32 v220, s50, v219
	ds_add_f64 v220, v[200:201] offset:32768
	ds_add_f64 v220, v[202:203] offset:33280
	ds_add_f64 v220, v[204:205] offset:33792
	ds_add_f64 v220, v[206:207] offset:34304
	v_mov_b32_e32 v200, 0
	v_mov_b32_e32 v201, 0
	v_mov_b32_e32 v202, 0
	v_mov_b32_e32 v203, 0
	v_mov_b32_e32 v204, 0
	v_mov_b32_e32 v205, 0
	v_mov_b32_e32 v206, 0
	v_mov_b32_e32 v207, 0
	s_mov_b32 s50, s77
	s_branch .Lg2_B8_cont17

.Lg_nocopy:
	s_waitcnt vmcnt(0)
	s_waitcnt vmcnt(0)
	v_mul_f32_e32 v150, v62, v62
	v_mul_f32_e32 v151, v63, v63
	v_mul_f32_e32 v152, v64, v64
	v_mul_f32_e32 v153, v65, v65
	v_fmac_f32_e32 v150, v58, v58
	v_fmac_f32_e32 v151, v59, v59
	v_fmac_f32_e32 v152, v60, v60
	v_fmac_f32_e32 v153, v61, v61
	v_fmac_f32_e32 v150, v54, v54
	v_fmac_f32_e32 v151, v55, v55
	v_fmac_f32_e32 v152, v56, v56
	v_fmac_f32_e32 v153, v57, v57
	v_fmac_f32_e32 v150, v50, v50
	v_fmac_f32_e32 v151, v51, v51
	v_fmac_f32_e32 v152, v52, v52
	v_fmac_f32_e32 v153, v53, v53
	v_fmac_f32_e32 v150, v46, v46
	v_fmac_f32_e32 v151, v47, v47
	v_fmac_f32_e32 v152, v48, v48
	v_fmac_f32_e32 v153, v49, v49
	v_fmac_f32_e32 v150, v42, v42
	v_fmac_f32_e32 v151, v43, v43
	v_fmac_f32_e32 v152, v44, v44
	v_fmac_f32_e32 v153, v45, v45
	v_fmac_f32_e32 v150, v38, v38
	v_fmac_f32_e32 v151, v39, v39
	v_fmac_f32_e32 v152, v40, v40
	v_fmac_f32_e32 v153, v41, v41
	v_fmac_f32_e32 v150, v34, v34
	v_fmac_f32_e32 v151, v35, v35
	v_fmac_f32_e32 v152, v36, v36
	v_fmac_f32_e32 v153, v37, v37
	v_fmac_f32_e32 v150, v30, v30
	v_fmac_f32_e32 v151, v31, v31
	v_fmac_f32_e32 v152, v32, v32
	v_fmac_f32_e32 v153, v33, v33
	v_fmac_f32_e32 v150, v26, v26
	v_fmac_f32_e32 v151, v27, v27
	v_fmac_f32_e32 v152, v28, v28
	v_fmac_f32_e32 v153, v29, v29
	v_fmac_f32_e32 v150, v22, v22
	v_fmac_f32_e32 v151, v23, v23
	v_fmac_f32_e32 v152, v24, v24
	v_fmac_f32_e32 v153, v25, v25
	v_fmac_f32_e32 v150, v18, v18
	v_fmac_f32_e32 v151, v19, v19
	v_fmac_f32_e32 v152, v20, v20
	v_fmac_f32_e32 v153, v21, v21
	v_fmac_f32_e32 v150, v14, v14
	v_fmac_f32_e32 v151, v15, v15
	v_fmac_f32_e32 v152, v16, v16
	v_fmac_f32_e32 v153, v17, v17
	v_fmac_f32_e32 v150, v10, v10
	v_fmac_f32_e32 v151, v11, v11
	v_fmac_f32_e32 v152, v12, v12
	v_fmac_f32_e32 v153, v13, v13
	v_fmac_f32_e32 v150, v6, v6
	v_fmac_f32_e32 v151, v7, v7
	v_fmac_f32_e32 v152, v8, v8
	v_fmac_f32_e32 v153, v9, v9
	v_fmac_f32_e32 v150, v2, v2
	v_fmac_f32_e32 v151, v3, v3
	v_fmac_f32_e32 v152, v4, v4
	v_fmac_f32_e32 v153, v5, v5
	v_add_f32_e32 v150, v150, v151
	v_add_f32_e32 v152, v152, v153
	v_add_f32_e32 v150, v150, v152
	v_mbcnt_lo_u32_b32 v151, -1, 0
	v_mbcnt_hi_u32_b32 v151, -1, v151
	v_xor_b32_e32 v152, 16, v151
	v_lshlrev_b32_e32 v152, 2, v152
	ds_bpermute_b32 v152, v152, v150
	v_xor_b32_e32 v153, 32, v151
	v_lshlrev_b32_e32 v153, 2, v153
	s_waitcnt lgkmcnt(0)
	v_add_f32_e32 v150, v150, v152
	ds_bpermute_b32 v153, v153, v150
	v_add_u32_e32 v152, s24, v1
	v_lshlrev_b32_e32 v152, 2, v152
	v_add_u32_e32 v152, 0x11300, v152
	v_cmp_gt_u32_e32 vcc, 16, v1
	s_and_saveexec_b64 s[30:31], vcc
	s_waitcnt lgkmcnt(0)
	v_add_f32_e32 v150, v150, v153
	ds_write_b32 v152, v150
	s_mov_b64 exec, s[30:31]
	v_and_b32_e32 v138, 15, v0
	v_or_b32_e32 v134, s24, v138
	v_lshlrev_b32_e32 v135, 3, v1
	v_lshlrev_b32_e32 v139, 2, v1
	v_bfe_u32 v140, v0, 4, 2
	v_cmp_eq_u32_e64 s[2:3], 0, v1
